# ssm_pre conv tiles: raw-row base pointer selected from two pointers loaded once before the tile loop instead of a scalar kernarg load per tile
# baseline (speedup 1.0000x reference)
; __device__ __forceinline__ float bflo(uint32_t w) { return __uint_as_float(w << 16); }
; __device__ __forceinline__ float bfhi(uint32_t w) { return __uint_as_float(w & 0xffff0000u); }
; __device__ __forceinline__ float silu_f(float v) { return v / (1.f + __expf(-v)); }
; __device__ void ssm_pre_tile(KParams& p, int task, char* smem) {
;   const bool isx = task < 3072;
;   const int u = isx ? task : task - 3072;
;   const int ntt = isx ? 32 : 4;
;   const int ct = u % 24, tt = (u / 24) % ntt, b = u / (24 * ntt);
;   const int seqlen = isx ? L : CTX;
;   const bf16_t* raw = (isx ? p.xbcraw : p.xbcraw_c) + (size_t)b * seqlen * DXBC;
;   const int l0 = tt * 64, c0 = ct * 64, tid = threadIdx.x;
;   float (*rt)[68] = reinterpret_cast<float (*)[68]>(smem);
;   float (*at)[65] = reinterpret_cast<float (*)[65]>(smem + 66 * 68 * 4);
;   __syncthreads();
;   {
;     uint2 v[5];
; #pragma unroll
;     for (int k = 0; k < 5; ++k) {
;       const int i = tid + k * NTHREADS, r = i >> 4, c4 = i & 15, l = l0 - 1 + r;
;       v[k] = (i < 66 * 16 && l >= 0 && l < seqlen) ? *reinterpret_cast<const uint2*>(raw + (size_t)l * DXBC + c0 + c4 * 4) : uint2{0u, 0u};
;     }
; #pragma unroll
;     for (int k = 0; k < 5; ++k) {
;       const int i = tid + k * NTHREADS, r = i >> 4, c4 = i & 15;
;       if (i < 66 * 16) *reinterpret_cast<float4*>(&rt[r][c4 * 4]) = float4{bflo(v[k].x), bfhi(v[k].x), bflo(v[k].y), bfhi(v[k].y)};
;     }
;   }
;   __syncthreads();
;   {
;     const int cc = tid & 63, c = c0 + cc;
;     const float w0 = p.conv_w[c], w1 = p.conv_w[DXBC + c], w2 = p.conv_w[2 * DXBC + c], cb = p.conv_b[c];
; #pragma unroll 4
;     for (int r = tid >> 6; r < 64; r += 4) at[r][cc] = silu_f(cb + rt[r][cc] * w0 + rt[r + 1][cc] * w1 + rt[r + 2][cc] * w2);
;   }
;   __syncthreads();
;   const size_t trow0 = isx ? ((size_t)b * L + l0) : ((size_t)T + (size_t)b * CTX + l0);
; #pragma unroll
;   for (int k = 0; k < 4; ++k) {
;     const int i = tid + k * NTHREADS, r = i >> 4, c4 = (i & 15) * 4;
;     uint2 o; o.x = pack2(at[r][c4], at[r][c4 + 1]); o.y = pack2(at[r][c4 + 2], at[r][c4 + 3]);
;     *reinterpret_cast<uint2*>(p.act_tm + (trow0 + r) * DXBC + c0 + c4) = o;
.LBB0_633:
	s_or_b64 exec, exec, s[10:11]
	s_cmpk_gt_i32 s2, 0xd7f
	s_cbranch_scc1 .LBB0_666
	v_or_b32_e32 v2, 0x100, v0
	s_load_dwordx4 s[16:19], s[14:15], 0x60
	s_load_dwordx4 s[60:63], s[14:15], 0x1b0
	s_load_dwordx2 s[20:21], s[14:15], 0x1f0
	v_lshrrev_b32_e32 v4, 4, v2
	v_or_b32_e32 v2, 0x200, v0
	v_lshlrev_b32_e32 v12, 2, v194
	s_movk_i32 s40, 0x110
	v_lshrrev_b32_e32 v6, 4, v2
	v_or_b32_e32 v2, 0x300, v0
	v_mad_u32_u24 v25, v192, s40, v12
	v_mul_i32_i24_e32 v13, -12, v192
	v_lshrrev_b32_e32 v8, 4, v2
	v_or_b32_e32 v2, 0x400, v0
	s_movk_i32 s12, 0x420
	v_mad_u32_u24 v26, v4, s40, v12
	v_mul_i32_i24_e32 v14, -12, v4
	v_add_u32_e32 v13, v25, v13
	s_waitcnt lgkmcnt(0)
	v_mov_b32_e32 v3, 0
	v_lshrrev_b32_e32 v24, 4, v2
	v_cmp_gt_u32_e64 s[12:13], s12, v2
	v_mad_u32_u24 v27, v6, s40, v12
	v_lshlrev_b32_e32 v2, 1, v194
	v_mul_i32_i24_e32 v15, -12, v6
	v_add_u32_e32 v35, 0x4620, v13
	v_add_u32_e32 v36, 0x4628, v13
	v_add_u32_e32 v13, v26, v14
	v_mad_u32_u24 v28, v8, s40, v12
	v_lshl_add_u64 v[10:11], s[20:21], 0, v[2:3]
	v_mul_i32_i24_e32 v16, -12, v8
	v_lshl_or_b32 v2, v194, 8, v12
	v_add_u32_e32 v37, 0x4620, v13
	v_add_u32_e32 v38, 0x4628, v13
	v_add_u32_e32 v13, v27, v15
	s_movk_i32 s6, 0x320
	s_movk_i32 s8, 0x220
	s_movk_i32 s10, 0x120
	v_mad_u32_u24 v29, v24, s40, v12
	v_lshl_add_u32 v12, v192, 2, v2
	v_lshl_add_u32 v17, v4, 2, v2
	v_lshl_add_u32 v18, v6, 2, v2
	v_lshl_add_u32 v19, v8, 2, v2
	v_mul_u32_u24_e32 v32, 0x104, v143
	s_movk_i32 s20, 0x4620
	v_add_u32_e32 v39, 0x4620, v13
	v_add_u32_e32 v40, 0x4628, v13
	v_add_u32_e32 v13, v28, v16
	v_cmp_gt_u32_e64 s[6:7], s6, v0
	v_cmp_gt_u32_e64 s[8:9], s8, v0
	v_cmp_gt_u32_e64 s[10:11], s10, v0
	v_mov_b32_e32 v193, v3
	v_mov_b32_e32 v5, v3
	v_mov_b32_e32 v7, v3
	v_mov_b32_e32 v9, v3
	v_mul_u32_u24_e32 v30, 0x110, v143
	v_mad_u32_u24 v31, v143, s40, v190
	s_movk_i32 s41, 0x104
	v_add3_u32 v33, v32, v190, s20
	v_add_u32_e32 v34, 0x4620, v190
	s_movk_i32 s42, 0xc00
	s_movk_i32 s43, 0x60
	s_movk_i32 s46, 0x800
	s_movk_i32 s47, 0x1b0
	v_lshlrev_b32_e32 v2, 1, v194
	s_mov_b64 s[20:21], 0
	v_add_u32_e32 v41, 0x4620, v13
	v_add_u32_e32 v42, 0x4628, v13
	s_movk_i32 s50, 0x1f8
	v_add_u32_e32 v43, 0x4400, v12
	v_add_u32_e32 v44, 0x4800, v12
	v_add_u32_e32 v45, 0x4400, v17
	v_add_u32_e32 v46, 0x4800, v17
	v_add_u32_e32 v47, 0x4400, v18
	v_add_u32_e32 v48, 0x4800, v18
	v_add_u32_e32 v49, 0x4400, v19
	v_add_u32_e32 v50, 0x4800, v19
	s_mov_b32 s51, s2
	s_branch .LBB0_636

; __device__ void ssm_pre_tile(KParams& p, int task, char* smem) {
;   const bool isx = task < 3072;
;   const int u = isx ? task : task - 3072;
;   const int ntt = isx ? 32 : 4;
;   const int ct = u % 24, tt = (u / 24) % ntt, b = u / (24 * ntt);
;   const int seqlen = isx ? L : CTX;
;   const bf16_t* raw = (isx ? p.xbcraw : p.xbcraw_c) + (size_t)b * seqlen * DXBC;
;   const int l0 = tt * 64, c0 = ct * 64, tid = threadIdx.x;
;   float (*rt)[68] = reinterpret_cast<float (*)[68]>(smem);
;   float (*at)[65] = reinterpret_cast<float (*)[65]>(smem + 66 * 68 * 4);
;   __syncthreads();
;   {
;     uint2 v[5];
; #pragma unroll
;     for (int k = 0; k < 5; ++k) {
;       const int i = tid + k * NTHREADS, r = i >> 4, c4 = i & 15, l = l0 - 1 + r;
;       v[k] = (i < 66 * 16 && l >= 0 && l < seqlen) ? *reinterpret_cast<const uint2*>(raw + (size_t)l * DXBC + c0 + c4 * 4) : uint2{0u, 0u};
.LBB0_636:
	s_cmpk_gt_i32 s51, 0xbff
	s_cselect_b64 s[30:31], -1, 0
	s_add_i32 s26, s51, 0xfffff400
	s_cmpk_lt_i32 s51, 0xc00
	s_cselect_b64 s[22:23], -1, 0
	s_and_b64 s[24:25], s[22:23], exec
	s_cselect_b32 s25, 32, 4
	v_cvt_f32_ubyte0_e32 v12, s25
	v_rcp_iflag_f32_e32 v12, v12
	s_cselect_b32 s24, s51, s26
	s_mul_hi_i32 s26, s24, 0x2aaaaaab
	s_cselect_b32 s27, 0x300, s43
	v_mul_f32_e32 v12, 0x4f7ffffe, v12
	v_cvt_u32_f32_e32 v12, v12
	s_cselect_b32 s29, s46, 0x100
	s_cselect_b32 s52, 11, 8
	s_cselect_b32 s28, s47, 0x1b8
	s_lshr_b32 s36, s26, 31
	s_ashr_i32 s26, s26, 2
	s_sub_i32 s37, 0, s25
	v_readfirstlane_b32 s38, v12
	s_add_i32 s26, s26, s36
	s_mul_i32 s37, s37, s38
	v_cvt_f32_u32_e32 v12, s27
	s_mul_i32 s36, s26, 24
	s_mul_hi_u32 s37, s38, s37
	s_sub_i32 s53, s24, s36
	s_ashr_i32 s36, s26, 31
	s_abs_i32 s26, s26
	s_add_i32 s38, s38, s37
	s_mul_hi_u32 s37, s26, s38
	s_mul_i32 s37, s37, s25
	v_rcp_iflag_f32_e32 v12, v12
	s_sub_i32 s26, s26, s37
	s_sub_i32 s37, s26, s25
	s_cmp_ge_u32 s26, s25
	s_cselect_b32 s26, s37, s26
	v_mul_f32_e32 v12, 0x4f7ffffe, v12
	s_sub_i32 s37, s26, s25
	v_cvt_u32_f32_e32 v12, v12
	s_cmp_ge_u32 s26, s25
	s_cselect_b32 s25, s37, s26
	s_xor_b32 s25, s25, s36
	s_sub_i32 s38, s25, s36
	s_sub_i32 s26, 0, s27
	v_readfirstlane_b32 s36, v12
	s_mul_i32 s26, s26, s36
	s_mul_hi_u32 s26, s36, s26
	s_ashr_i32 s25, s24, 31
	s_abs_i32 s24, s24
	s_add_i32 s36, s36, s26
	s_mul_hi_u32 s26, s24, s36
	s_mul_i32 s36, s26, s27
	s_sub_i32 s24, s24, s36
	s_add_i32 s36, s26, 1
	s_sub_i32 s37, s24, s27
	s_cmp_ge_u32 s24, s27
	s_cselect_b32 s26, s36, s26
	s_cselect_b32 s24, s37, s24
	s_add_i32 s36, s26, 1
	s_cmp_ge_u32 s24, s27
	s_cselect_b32 s24, s36, s26
	s_xor_b32 s24, s24, s25
	s_sub_i32 s26, s24, s25
	s_cmp_lg_u32 s22, 0
	s_cselect_b32 s24, s60, s62
	s_cselect_b32 s25, s61, s63
	s_ashr_i32 s27, s26, 31
	s_lshl_b64 s[36:37], s[26:27], s52
	s_mul_i32 s28, s37, 0xc00
	s_mul_hi_u32 s37, s36, 0xc00
	s_add_i32 s37, s37, s28
	s_mul_i32 s28, s36, 0xc00
	s_waitcnt lgkmcnt(0)
	s_add_u32 s39, s24, s28
	s_addc_u32 s54, s25, s37
	s_lshl_b32 s24, s53, 6
	s_lshl_b32 s28, s38, 6
	s_ashr_i32 s25, s24, 31
	s_add_i32 s38, s28, -1
	s_lshl_b64 s[36:37], s[24:25], 1
	s_add_u32 s36, s39, s36
	s_addc_u32 s37, s54, s37
	v_add_u32_e32 v12, s38, v192
	v_lshl_add_u64 v[22:23], s[36:37], 0, v[2:3]
	v_cmp_gt_u32_e32 vcc, s29, v12
	v_mov_b64_e32 v[14:15], 0
	v_mov_b64_e32 v[18:19], 0
	s_barrier
	s_and_saveexec_b64 s[36:37], vcc
	s_cbranch_execz .LBB0_638
	v_mad_u64_u32 v[12:13], s[54:55], v12, s42, v[22:23]
	global_load_dwordx2 v[18:19], v[12:13], off
